# v16: v15 plus P-pack conversions moved from the loaded QK gaps to the last four gaps of the MLA QK section
# baseline (speedup 1.0000x reference)
; __device__ __forceinline__ unsigned cvt_pk_bf16(float lo, float hi) { unsigned r; asm volatile("v_cvt_pk_bf16_f32 %0, %1, %2" : "=v"(r) : "v"(lo), "v"(hi)); return r; }
; __device__ __forceinline__ s16x4 vtr(lds_cptr p) { return __builtin_bit_cast(s16x4, __builtin_amdgcn_ds_read_tr16_b64_v4i16((LAS v4i16_t*)p)); }
; #define SFENCE() __builtin_amdgcn_sched_barrier(0)
; template <bool FOX>
; __device__ __forceinline__ void attn_unit(const Args& A, int b, int h, int qb, LAS char* shm, LAS float* dg) {
;     ...
;           const lds_cptr vp = vp0 + ((t - 1) % NS) * VSLOT; float sa = 0.f, sb = 0.f;
; #pragma unroll
;           for (int g = 0; g < 2 * NQ; ++g) {
;               if (!FOX && g == 0) c0 = __builtin_amdgcn_mfma_f32_32x32x16_bf16(kf[0], qr[0], negm, 0, 0, 0);
;               else if (!FOX && g == 1) c1 = __builtin_amdgcn_mfma_f32_32x32x16_bf16(kf[1], qr[0], negm, 0, 0, 0);
;               else if (g & 1) c1 = __builtin_amdgcn_mfma_f32_32x32x16_bf16(kf[g], qr[g >> 1], c1, 0, 0, 0); else c0 = __builtin_amdgcn_mfma_f32_32x32x16_bf16(kf[g], qr[g >> 1], c0, 0, 0, 0);
;               if (g < 8) { const int i = (g >> 1) + 4 * (g & 1); vlo[i] = vtr(vp + (i >> 2) * 4096 + (i & 3) * 1024); vhi[i] = vtr(vp + (i >> 2) * 4096 + (i & 3) * 1024 + 512);
;                   if (g < 4) { sa += pp0[4 * g]; sb += pp0[4 * g + 1]; sa += pp0[4 * g + 2]; sb += pp0[4 * g + 3]; } else { sa += pp1[4 * g - 16]; sb += pp1[4 * g - 15]; sa += pp1[4 * g - 14]; sb += pp1[4 * g - 13]; }
;                   asm volatile("" : "+v"(sa), "+v"(sb)); }
;               { constexpr int G0 = FOX ? 0 : 4; if (g >= G0) { const int q = 2 * (g - G0);
; #pragma unroll
;                   for (int k = 0; k < 2; ++k) { const int w = q + k; const unsigned pkd = w < 8 ? cvt_pk_bf16(pp0[2 * w], pp0[2 * w + 1]) : cvt_pk_bf16(pp1[2 * w - 16], pp1[2 * w - 15]); pw[w >> 2][w & 3] = pkd; } } }
;               SFENCE();
;           }
;           lrun += sa + sb; }
.LBB0_835:
	s_add_i32 s27, s42, 0x8000
	v_mfma_f32_32x32x16_bf16 v[114:129], v[206:209], v[138:141], v[82:97]
	s_and_b32 s27, s27, 0x6000
	v_add_u32_e32 v3, s27, v247
	ds_read_b64_tr_b16 v[206:207], v3 offset:49152
	ds_read_b64_tr_b16 v[208:209], v3 offset:49664
	v_add_f32_e32 v4, 0, v67
	v_add_f32_e32 v5, 0, v66
	v_add_f32_e32 v4, v69, v4
	v_add_f32_e32 v5, v68, v5
	v_mfma_f32_32x32x16_bf16 v[98:113], v[194:197], v[138:141], v[82:97]
	ds_read_b64_tr_b16 v[194:195], v3 offset:53248
	ds_read_b64_tr_b16 v[196:197], v3 offset:53760
	v_add_f32_e32 v4, v71, v4
	v_add_f32_e32 v5, v70, v5
	v_add_f32_e32 v4, v73, v4
	v_add_f32_e32 v5, v72, v5
	v_mfma_f32_32x32x16_bf16 v[114:129], v[202:205], v[142:145], v[114:129]
	ds_read_b64_tr_b16 v[202:203], v3 offset:50176
	ds_read_b64_tr_b16 v[204:205], v3 offset:50688
	v_add_f32_e32 v4, v75, v4
	v_add_f32_e32 v5, v74, v5
	v_add_f32_e32 v4, v77, v4
	v_add_f32_e32 v5, v76, v5
	v_mfma_f32_32x32x16_bf16 v[98:113], v[186:189], v[142:145], v[98:113]
	ds_read_b64_tr_b16 v[214:215], v3 offset:54272
	ds_read_b64_tr_b16 v[216:217], v3 offset:54784
	v_add_f32_e32 v4, v79, v4
	v_add_f32_e32 v5, v78, v5
	v_add_f32_e32 v4, v81, v4
	v_add_f32_e32 v5, v80, v5
	v_mfma_f32_32x32x16_bf16 v[114:129], v[198:201], v[146:149], v[114:129]
	ds_read_b64_tr_b16 v[210:211], v3 offset:51200
	ds_read_b64_tr_b16 v[212:213], v3 offset:51712
	v_add_f32_e32 v4, v51, v4
	v_add_f32_e32 v5, v50, v5
	v_add_f32_e32 v4, v53, v4
	v_add_f32_e32 v5, v52, v5
	v_mfma_f32_32x32x16_bf16 v[98:113], v[182:185], v[146:149], v[98:113]
	ds_read_b64_tr_b16 v[12:13], v3 offset:55296
	ds_read_b64_tr_b16 v[14:15], v3 offset:55808
	v_add_f32_e32 v4, v55, v4
	v_add_f32_e32 v5, v54, v5
	v_add_f32_e32 v4, v57, v4
	v_add_f32_e32 v5, v56, v5
	v_mfma_f32_32x32x16_bf16 v[114:129], v[190:193], v[150:153], v[114:129]
	ds_read_b64_tr_b16 v[8:9], v3 offset:52224
	ds_read_b64_tr_b16 v[10:11], v3 offset:52736
	v_add_f32_e32 v4, v59, v4
	v_add_f32_e32 v16, v61, v4
	v_add_f32_e32 v4, v58, v5
	v_add_f32_e32 v17, v60, v4
	v_mfma_f32_32x32x16_bf16 v[98:113], v[170:173], v[150:153], v[98:113]
	ds_read_b64_tr_b16 v[4:5], v3 offset:56320
	ds_read_b64_tr_b16 v[6:7], v3 offset:56832
	v_add_f32_e32 v3, v63, v16
	v_add_f32_e32 v16, v62, v17
	v_add_f32_e32 v3, v65, v3
	v_add_f32_e32 v16, v64, v16
	v_mfma_f32_32x32x16_bf16 v[114:129], v[178:181], v[154:157], v[114:129]
	v_cvt_pk_bf16_f32 v178, v50, v51
	v_cvt_pk_bf16_f32 v179, v52, v53
	v_cvt_pk_bf16_f32 v186, v66, v67
	v_cvt_pk_bf16_f32 v187, v68, v69
	v_mfma_f32_32x32x16_bf16 v[98:113], v[166:169], v[154:157], v[98:113]
	v_cvt_pk_bf16_f32 v180, v54, v55
	v_cvt_pk_bf16_f32 v181, v56, v57
	v_cvt_pk_bf16_f32 v188, v70, v71
	v_cvt_pk_bf16_f32 v189, v72, v73
	v_mfma_f32_32x32x16_bf16 v[114:129], v[174:177], v[158:161], v[114:129]
	v_cvt_pk_bf16_f32 v218, v58, v59
	v_cvt_pk_bf16_f32 v219, v60, v61
	v_cvt_pk_bf16_f32 v182, v74, v75
	v_cvt_pk_bf16_f32 v183, v76, v77
	v_mfma_f32_32x32x16_bf16 v[98:113], v[162:165], v[158:161], v[98:113]
	v_cvt_pk_bf16_f32 v220, v62, v63
	v_cvt_pk_bf16_f32 v221, v64, v65
	v_cvt_pk_bf16_f32 v184, v78, v79
	v_cvt_pk_bf16_f32 v185, v80, v81
	v_add_f32_e32 v3, v3, v16
	s_cmp_lg_u32 s98, 0
	s_cbranch_scc1 .Lmla_fixed_ref
	s_nop 9
	v_max_f32_e32 v16, v115, v115
	v_max_f32_e32 v17, v114, v114
	v_max_f32_e32 v16, v17, v16
	v_max3_f32 v17, v116, v117, v99
	v_max3_f32 v16, v16, v98, v100
	v_max3_f32 v16, v16, v101, v118
	v_max3_f32 v17, v17, v120, v121
	v_max3_f32 v16, v16, v119, v102
	v_max3_f32 v17, v17, v104, v105
	v_max3_f32 v16, v16, v103, v122
	v_max3_f32 v17, v17, v124, v125
	v_max3_f32 v16, v16, v123, v106
	v_max3_f32 v17, v17, v108, v109
	v_max3_f32 v16, v16, v107, v126
	v_max3_f32 v17, v17, v128, v129
	v_max3_f32 v16, v16, v127, v110
	v_max3_f32 v17, v17, v112, v113
	v_add_f32_e32 v246, v246, v3
	v_max3_f32 v3, v16, v111, v17
	v_mov_b32_e32 v16, v3
	s_nop 1
	v_permlane32_swap_b32_e32 v3, v16
	v_max_f32_e32 v16, v16, v16
	v_max_f32_e32 v3, v3, v3
	v_max_f32_e32 v3, v3, v16
	v_cmp_lt_f32_e32 vcc, s95, v3
	s_cmp_lg_u64 vcc, 0
	s_cselect_b64 s[60:61], -1, 0
	s_cbranch_vccz .LBB0_839
	v_max_f32_e32 v3, v3, v3
	v_max_f32_e32 v3, 0, v3
	v_exp_f32_e64 v16, -v3
	v_add_f32_e32 v249, v249, v3
	v_xor_b32_e32 v82, 0x80000000, v249
	v_mov_b32_e32 v83, v82
	v_mov_b32_e32 v84, v82
	v_mov_b32_e32 v85, v82
	v_mov_b32_e32 v86, v82
	v_mov_b32_e32 v87, v82
	v_mov_b32_e32 v88, v82
	v_mov_b32_e32 v89, v82
	v_mov_b32_e32 v90, v82
	v_mov_b32_e32 v91, v82
	v_mov_b32_e32 v92, v82
	v_mov_b32_e32 v93, v82
	v_mov_b32_e32 v94, v82
	v_mov_b32_e32 v95, v82
	v_mov_b32_e32 v96, v82
	v_mov_b32_e32 v97, v82
	s_and_saveexec_b64 s[64:65], s[24:25]
	ds_write_b32 v245, v16
	s_or_b64 exec, exec, s[64:65]
	v_sub_f32_e32 v129, v129, v3
	v_sub_f32_e32 v128, v128, v3
	v_sub_f32_e32 v127, v127, v3
	v_sub_f32_e32 v126, v126, v3
	v_sub_f32_e32 v125, v125, v3
	v_sub_f32_e32 v124, v124, v3
	v_sub_f32_e32 v123, v123, v3
	v_sub_f32_e32 v122, v122, v3
	v_sub_f32_e32 v121, v121, v3
	v_sub_f32_e32 v120, v120, v3
	v_sub_f32_e32 v119, v119, v3
	v_sub_f32_e32 v118, v118, v3
	v_sub_f32_e32 v117, v117, v3
	v_sub_f32_e32 v116, v116, v3
	v_sub_f32_e32 v115, v115, v3
	v_sub_f32_e32 v114, v114, v3
	v_sub_f32_e32 v113, v113, v3
	v_sub_f32_e32 v112, v112, v3
	v_sub_f32_e32 v111, v111, v3
	v_sub_f32_e32 v110, v110, v3
	v_sub_f32_e32 v109, v109, v3
	v_sub_f32_e32 v108, v108, v3
	v_sub_f32_e32 v107, v107, v3
	v_sub_f32_e32 v106, v106, v3
	v_sub_f32_e32 v105, v105, v3
	v_sub_f32_e32 v104, v104, v3
	v_sub_f32_e32 v103, v103, v3
	v_sub_f32_e32 v102, v102, v3
	v_sub_f32_e32 v101, v101, v3
	v_sub_f32_e32 v100, v100, v3
	v_sub_f32_e32 v99, v99, v3
	v_sub_f32_e32 v98, v98, v3
	v_mul_f32_e32 v246, v246, v16
	s_branch .LBB0_839
